# P4 pass loops: waves 4-7 (the second wave on each SIMD) start each selection pass half a tile later (s_sleep) so the two waves of a SIMD are out of phase between their MFMA and VALU sections
# speedup vs baseline: 1.0018x; 1.0018x over previous
; #define LAS __attribute__((address_space(3)))
; __device__ __forceinline__ bf16 f2bf(float f) { unsigned u = __float_as_uint(f); return (bf16)((u + 0x7fffu + ((u >> 16) & 1u)) >> 16); }
; __device__ __forceinline__ bool run_unit2(LAS unsigned char* lds, const bf16* y0, const float* aux, unsigned* maskg, int b, int g, int tid_in, int wave, int lane) {
;     ...
;     for (int i = tid; i < (OFF2_TB) / 4; i += NTHR) ((LAS unsigned*)lds)[i] = 0u;
;     if (tid < 32) { ((LAS unsigned*)(lds + OFF2_CNT))[tid] = 0u; }
;     if (tid == 0) ((LAS int*)(lds + OFF2_FLAG))[0] = 0;
;     bf16x8 qf[4][4];
;     {
;         const bf16* qp = y0 + (rowbase + t0 + r) * (size_t)Y0P + Y0_IQ + 8 * h2;
; #pragma unroll
;         for (int hd = 0; hd < 4; ++hd)
; #pragma unroll
;             for (int s = 0; s < 4; ++s) qf[hd][s] = *(const bf16x8*)(qp + hd * 64 + 16 * s);
;     }
;     const f32x4 w4 = *(const f32x4*)(aux + (rowbase + t0 + r) * 16 + 8);
;     f32x4 lo4, hi4;
; #pragma unroll
;     for (int hd = 0; hd < 4; ++hd) {
;         const float wsc = w4[hd] * 0.0625f;
;         lo4[hd] = (w4[hd] >= 0.f) ? 0.f : -INFINITY; hi4[hd] = (w4[hd] >= 0.f) ? INFINITY : 0.f;
; #pragma unroll
;         for (int s = 0; s < 4; ++s) {
;             bf16x8 a = qf[hd][s];
; #pragma unroll
;             for (int j = 0; j < 8; ++j) a[j] = (short)f2bf(__uint_as_float(((unsigned)(unsigned short)a[j]) << 16) * wsc);
;             qf[hd][s] = a;
;         }
;     }
.LBB0_779:
	s_or_b64 exec, exec, s[2:3]
	v_cmp_gt_i32_e32 vcc, 32, v206
	s_and_saveexec_b64 s[2:3], vcc
	v_lshl_add_u32 v0, v206, 2, 0
	v_add_u32_e32 v0, 0x18200, v0
	ds_write_b32 v0, v177
	s_or_b64 exec, exec, s[2:3]
	v_cmp_eq_u32_e32 vcc, 0, v206
	s_and_saveexec_b64 s[2:3], vcc
	v_mov_b32_e32 v0, s88
	ds_write_b32 v0, v177
	s_or_b64 exec, exec, s[2:3]
	s_andn2_b32 s64, 0xff, s0
	s_lshr_b32 s66, s0, 8
	v_and_b32_e32 v218, 31, v217
	s_lshl_b32 s41, s64, 5
	v_ashrrev_i32_e32 v219, 5, v217
	s_lshl_b64 s[76:77], s[66:67], 13
	v_or_b32_e32 v211, s41, v218
	v_or_b32_e32 v0, s76, v211
	v_mov_b64_e32 v[2:3], s[44:45]
	s_waitcnt vmcnt(0)
	v_lshlrev_b32_e32 v48, 3, v219
	v_mov_b32_e32 v1, s77
	v_mad_u64_u32 v[2:3], s[0:1], v0, s33, v[2:3]
	v_ashrrev_i32_e32 v49, 31, v48
	v_mad_u32_u24 v3, s77, v187, v3
	v_lshlrev_b64 v[50:51], 1, v[48:49]
	v_lshlrev_b64 v[0:1], 6, v[0:1]
	v_lshl_add_u64 v[2:3], v[2:3], 0, v[50:51]
	v_lshl_add_u64 v[0:1], s[46:47], 0, v[0:1]
	global_load_dwordx4 v[16:19], v[0:1], off offset:32
	v_add_co_u32_e32 v0, vcc, s31, v2
	s_mul_i32 s78, s66, 0x3800000
	s_nop 0
	v_addc_co_u32_e32 v1, vcc, 0, v3, vcc
	global_load_dwordx4 v[52:55], v[0:1], off offset:2048
	v_lshl_add_u64 v[0:1], v[2:3], 0, s[28:29]
	global_load_dwordx4 v[56:59], v[0:1], off offset:32
	global_load_dwordx4 v[60:63], v[0:1], off offset:64
	global_load_dwordx4 v[76:79], v[0:1], off offset:96
	global_load_dwordx4 v[80:83], v[0:1], off offset:128
	global_load_dwordx4 v[44:47], v[0:1], off offset:160
	global_load_dwordx4 v[40:43], v[0:1], off offset:192
	global_load_dwordx4 v[36:39], v[0:1], off offset:224
	global_load_dwordx4 v[32:35], v[0:1], off offset:256
	global_load_dwordx4 v[28:31], v[0:1], off offset:288
	global_load_dwordx4 v[24:27], v[0:1], off offset:320
	global_load_dwordx4 v[20:23], v[0:1], off offset:352
	global_load_dwordx4 v[12:15], v[0:1], off offset:384
	global_load_dwordx4 v[8:11], v[0:1], off offset:416
	global_load_dwordx4 v[4:7], v[0:1], off offset:448
	s_nop 0
	global_load_dwordx4 v[0:3], v[0:1], off offset:480
	s_mul_hi_u32 s79, s66, 0x3800000
	s_add_u32 s0, s44, s78
	s_addc_u32 s1, s45, s79
	s_add_u32 s80, s0, 0x1a00
	s_addc_u32 s81, s1, 0
	v_mul_u32_u24_e32 v176, 0x1c00, v218
	v_readlane_b32 s0, v254, 24
	s_cmp_le_u32 s0, s64
	s_cselect_b64 s[82:83], -1, 0
	s_cmp_gt_u32 s0, s64
	s_waitcnt lgkmcnt(0)
	s_barrier
	s_waitcnt vmcnt(0)
	v_and_b32_e32 v71, 0xffff0000, v57
	v_lshlrev_b32_e32 v70, 16, v57
	v_and_b32_e32 v57, 0xffff0000, v58
	v_and_b32_e32 v73, 0xffff0000, v59
	v_lshlrev_b32_e32 v72, 16, v59
	v_mul_f32_e32 v84, 0x3d800000, v16
	v_cmp_le_f32_e32 vcc, 0, v16
	v_and_b32_e32 v65, 0xffff0000, v52
	v_lshlrev_b32_e32 v64, 16, v52
	v_and_b32_e32 v67, 0xffff0000, v53
	v_lshlrev_b32_e32 v66, 16, v53
	v_and_b32_e32 v53, 0xffff0000, v54
	v_lshlrev_b32_e32 v52, 16, v54
	v_and_b32_e32 v69, 0xffff0000, v55
	v_lshlrev_b32_e32 v68, 16, v55
	v_and_b32_e32 v55, 0xffff0000, v56
	v_lshlrev_b32_e32 v54, 16, v56
	v_lshlrev_b32_e32 v56, 16, v58
	v_pk_mul_f32 v[58:59], v[84:85], v[64:65] op_sel_hi:[0,1]
	v_pk_mul_f32 v[64:65], v[84:85], v[66:67] op_sel_hi:[0,1]
	v_pk_mul_f32 v[52:53], v[84:85], v[52:53] op_sel_hi:[0,1]
	v_pk_mul_f32 v[66:67], v[84:85], v[68:69] op_sel_hi:[0,1]
	v_pk_mul_f32 v[54:55], v[84:85], v[54:55] op_sel_hi:[0,1]
	v_pk_mul_f32 v[68:69], v[84:85], v[70:71] op_sel_hi:[0,1]
	v_pk_mul_f32 v[56:57], v[84:85], v[56:57] op_sel_hi:[0,1]
	v_pk_mul_f32 v[70:71], v[84:85], v[72:73] op_sel_hi:[0,1]
	v_bfe_u32 v16, v67, 16, 1
	v_bfe_u32 v72, v66, 16, 1
	v_bfe_u32 v73, v53, 16, 1
	v_bfe_u32 v74, v52, 16, 1
	v_bfe_u32 v75, v65, 16, 1
	v_bfe_u32 v85, v64, 16, 1
	v_bfe_u32 v86, v59, 16, 1
	v_bfe_u32 v87, v58, 16, 1
	v_add3_u32 v58, v58, v87, s73
	v_add3_u32 v59, v59, v86, s73
	v_add3_u32 v64, v64, v85, s73
	v_add3_u32 v65, v65, v75, s73
	v_add3_u32 v52, v52, v74, s73
	v_add3_u32 v53, v53, v73, s73
	v_add3_u32 v66, v66, v72, s73
	v_add3_u32 v16, v67, v16, s73
	v_bfe_u32 v88, v71, 16, 1
	v_bfe_u32 v89, v70, 16, 1
	v_bfe_u32 v90, v57, 16, 1
	v_bfe_u32 v91, v56, 16, 1
	v_perm_b32 v67, v16, v66, s72
	v_perm_b32 v66, v53, v52, s72
	v_perm_b32 v65, v65, v64, s72
	v_perm_b32 v64, v59, v58, s72
	v_bfe_u32 v16, v69, 16, 1
	v_bfe_u32 v52, v68, 16, 1
	v_bfe_u32 v53, v55, 16, 1
	v_bfe_u32 v58, v54, 16, 1
	v_add3_u32 v54, v54, v58, s73
	v_add3_u32 v53, v55, v53, s73
	v_add3_u32 v52, v68, v52, s73
	v_add3_u32 v16, v69, v16, s73
	v_add3_u32 v55, v56, v91, s73
	v_add3_u32 v56, v57, v90, s73
	v_add3_u32 v57, v70, v89, s73
	v_add3_u32 v58, v71, v88, s73
	v_perm_b32 v71, v58, v57, s72
	v_perm_b32 v70, v56, v55, s72
	v_perm_b32 v69, v16, v52, s72
	v_perm_b32 v68, v53, v54, s72
	v_and_b32_e32 v53, 0xffff0000, v60
	v_lshlrev_b32_e32 v52, 16, v60
	v_and_b32_e32 v55, 0xffff0000, v61
	v_lshlrev_b32_e32 v54, 16, v61
	v_and_b32_e32 v57, 0xffff0000, v62
	v_lshlrev_b32_e32 v56, 16, v62
	v_and_b32_e32 v59, 0xffff0000, v63
	v_lshlrev_b32_e32 v58, 16, v63
	v_pk_mul_f32 v[52:53], v[84:85], v[52:53] op_sel_hi:[0,1]
	v_pk_mul_f32 v[54:55], v[84:85], v[54:55] op_sel_hi:[0,1]
	v_pk_mul_f32 v[56:57], v[84:85], v[56:57] op_sel_hi:[0,1]
	v_pk_mul_f32 v[58:59], v[84:85], v[58:59] op_sel_hi:[0,1]
	v_bfe_u32 v16, v59, 16, 1
	v_bfe_u32 v60, v58, 16, 1
	v_bfe_u32 v61, v57, 16, 1
	v_bfe_u32 v62, v56, 16, 1
	v_bfe_u32 v63, v55, 16, 1
	v_bfe_u32 v72, v54, 16, 1
	v_bfe_u32 v73, v53, 16, 1
	v_bfe_u32 v74, v52, 16, 1
	v_add3_u32 v52, v52, v74, s73
	v_add3_u32 v53, v53, v73, s73
	v_add3_u32 v54, v54, v72, s73
	v_add3_u32 v55, v55, v63, s73
	v_add3_u32 v56, v56, v62, s73
	v_add3_u32 v57, v57, v61, s73
	v_add3_u32 v58, v58, v60, s73
	v_add3_u32 v16, v59, v16, s73
	v_perm_b32 v75, v16, v58, s72
; __device__ __forceinline__ bf16 f2bf(float f) { unsigned u = __float_as_uint(f); return (bf16)((u + 0x7fffu + ((u >> 16) & 1u)) >> 16); }
; __device__ __forceinline__ bool run_unit2(LAS unsigned char* lds, const bf16* y0, const float* aux, unsigned* maskg, int b, int g, int tid_in, int wave, int lane) {
;     ...
;     const f32x4 w4 = *(const f32x4*)(aux + (rowbase + t0 + r) * 16 + 8);
;     f32x4 lo4, hi4;
; #pragma unroll
;     for (int hd = 0; hd < 4; ++hd) {
;         const float wsc = w4[hd] * 0.0625f;
;         lo4[hd] = (w4[hd] >= 0.f) ? 0.f : -INFINITY; hi4[hd] = (w4[hd] >= 0.f) ? INFINITY : 0.f;
; #pragma unroll
;         for (int s = 0; s < 4; ++s) {
;             bf16x8 a = qf[hd][s];
; #pragma unroll
;             for (int j = 0; j < 8; ++j) a[j] = (short)f2bf(__uint_as_float(((unsigned)(unsigned short)a[j]) << 16) * wsc);
;             qf[hd][s] = a;
;         }
	v_perm_b32 v74, v57, v56, s72
	v_perm_b32 v73, v55, v54, s72
	v_perm_b32 v72, v53, v52, s72
	v_and_b32_e32 v53, 0xffff0000, v76
	v_lshlrev_b32_e32 v52, 16, v76
	v_and_b32_e32 v55, 0xffff0000, v77
	v_lshlrev_b32_e32 v54, 16, v77
	v_and_b32_e32 v57, 0xffff0000, v78
	v_lshlrev_b32_e32 v56, 16, v78
	v_and_b32_e32 v59, 0xffff0000, v79
	v_lshlrev_b32_e32 v58, 16, v79
	v_pk_mul_f32 v[52:53], v[84:85], v[52:53] op_sel_hi:[0,1]
	v_pk_mul_f32 v[54:55], v[84:85], v[54:55] op_sel_hi:[0,1]
	v_pk_mul_f32 v[56:57], v[84:85], v[56:57] op_sel_hi:[0,1]
	v_pk_mul_f32 v[58:59], v[84:85], v[58:59] op_sel_hi:[0,1]
	v_bfe_u32 v16, v59, 16, 1
	v_bfe_u32 v60, v58, 16, 1
	v_bfe_u32 v61, v57, 16, 1
	v_bfe_u32 v62, v56, 16, 1
	v_bfe_u32 v63, v55, 16, 1
	v_bfe_u32 v76, v54, 16, 1
	v_bfe_u32 v77, v53, 16, 1
	v_bfe_u32 v78, v52, 16, 1
	v_add3_u32 v52, v52, v78, s73
	v_add3_u32 v53, v53, v77, s73
	v_add3_u32 v54, v54, v76, s73
	v_add3_u32 v55, v55, v63, s73
	v_add3_u32 v56, v56, v62, s73
	v_add3_u32 v57, v57, v61, s73
	v_add3_u32 v58, v58, v60, s73
	v_add3_u32 v16, v59, v16, s73
	v_perm_b32 v79, v16, v58, s72
	v_perm_b32 v78, v57, v56, s72
	v_perm_b32 v77, v55, v54, s72
	v_perm_b32 v76, v53, v52, s72
	v_mul_f32_e32 v16, 0x3d800000, v17
	v_and_b32_e32 v53, 0xffff0000, v80
	v_lshlrev_b32_e32 v52, 16, v80
	v_and_b32_e32 v55, 0xffff0000, v81
	v_lshlrev_b32_e32 v54, 16, v81
	v_and_b32_e32 v57, 0xffff0000, v82
	v_lshlrev_b32_e32 v56, 16, v82
	v_pk_mul_f32 v[52:53], v[16:17], v[52:53] op_sel_hi:[0,1]
	v_pk_mul_f32 v[54:55], v[16:17], v[54:55] op_sel_hi:[0,1]
	v_pk_mul_f32 v[56:57], v[16:17], v[56:57] op_sel_hi:[0,1]
	v_and_b32_e32 v59, 0xffff0000, v83
	v_lshlrev_b32_e32 v58, 16, v83
	v_pk_mul_f32 v[58:59], v[16:17], v[58:59] op_sel_hi:[0,1]
	v_bfe_u32 v61, v57, 16, 1
	v_bfe_u32 v62, v56, 16, 1
	v_bfe_u32 v63, v55, 16, 1
	v_bfe_u32 v80, v54, 16, 1
	v_bfe_u32 v81, v53, 16, 1
	v_bfe_u32 v82, v52, 16, 1
	v_cndmask_b32_e64 v207, v188, 0, vcc
	v_cndmask_b32_e32 v208, 0, v189, vcc
	v_cmp_le_f32_e32 vcc, 0, v17
	v_bfe_u32 v17, v59, 16, 1
	v_add3_u32 v52, v52, v82, s73
	v_add3_u32 v53, v53, v81, s73
	v_add3_u32 v54, v54, v80, s73
	v_add3_u32 v55, v55, v63, s73
	v_add3_u32 v56, v56, v62, s73
	v_add3_u32 v57, v57, v61, s73
	v_bfe_u32 v60, v58, 16, 1
	v_add3_u32 v17, v59, v17, s73
	v_perm_b32 v82, v57, v56, s72
	v_perm_b32 v81, v55, v54, s72
	v_perm_b32 v80, v53, v52, s72
	v_and_b32_e32 v53, 0xffff0000, v44
	v_lshlrev_b32_e32 v52, 16, v44
	v_and_b32_e32 v55, 0xffff0000, v45
	v_lshlrev_b32_e32 v54, 16, v45
	v_and_b32_e32 v57, 0xffff0000, v47
	v_lshlrev_b32_e32 v56, 16, v47
	v_add3_u32 v58, v58, v60, s73
	v_pk_mul_f32 v[52:53], v[16:17], v[52:53] op_sel_hi:[0,1]
	v_pk_mul_f32 v[44:45], v[16:17], v[54:55] op_sel_hi:[0,1]
	v_and_b32_e32 v55, 0xffff0000, v46
	v_lshlrev_b32_e32 v54, 16, v46
	v_pk_mul_f32 v[46:47], v[16:17], v[56:57] op_sel_hi:[0,1]
	v_perm_b32 v83, v17, v58, s72
	v_pk_mul_f32 v[54:55], v[16:17], v[54:55] op_sel_hi:[0,1]
	v_bfe_u32 v17, v47, 16, 1
	v_bfe_u32 v56, v46, 16, 1
	v_bfe_u32 v61, v53, 16, 1
	v_bfe_u32 v62, v52, 16, 1
	v_bfe_u32 v59, v45, 16, 1
	v_bfe_u32 v60, v44, 16, 1
	v_add3_u32 v52, v52, v62, s73
	v_add3_u32 v53, v53, v61, s73
	v_add3_u32 v46, v46, v56, s73
	v_add3_u32 v17, v47, v17, s73
	v_add3_u32 v44, v44, v60, s73
	v_add3_u32 v45, v45, v59, s73
	v_perm_b32 v87, v17, v46, s72
	v_perm_b32 v84, v53, v52, s72
	v_and_b32_e32 v47, 0xffff0000, v41
	v_lshlrev_b32_e32 v46, 16, v41
	v_and_b32_e32 v53, 0xffff0000, v43
	v_lshlrev_b32_e32 v52, 16, v43
	v_bfe_u32 v57, v55, 16, 1
	v_bfe_u32 v58, v54, 16, 1
	v_perm_b32 v85, v45, v44, s72
	v_and_b32_e32 v45, 0xffff0000, v40
	v_lshlrev_b32_e32 v44, 16, v40
	v_pk_mul_f32 v[40:41], v[16:17], v[46:47] op_sel_hi:[0,1]
	v_and_b32_e32 v47, 0xffff0000, v42
	v_lshlrev_b32_e32 v46, 16, v42
	v_pk_mul_f32 v[42:43], v[16:17], v[52:53] op_sel_hi:[0,1]
	v_add3_u32 v54, v54, v58, s73
	v_add3_u32 v55, v55, v57, s73
	v_pk_mul_f32 v[44:45], v[16:17], v[44:45] op_sel_hi:[0,1]
	v_pk_mul_f32 v[46:47], v[16:17], v[46:47] op_sel_hi:[0,1]
	v_bfe_u32 v17, v43, 16, 1
	v_bfe_u32 v52, v42, 16, 1
	v_perm_b32 v86, v55, v54, s72
	v_bfe_u32 v55, v41, 16, 1
	v_bfe_u32 v56, v40, 16, 1
	v_bfe_u32 v57, v45, 16, 1
	v_bfe_u32 v58, v44, 16, 1
	v_add3_u32 v42, v42, v52, s73
	v_add3_u32 v17, v43, v17, s73
	v_add3_u32 v44, v44, v58, s73
	v_add3_u32 v45, v45, v57, s73
	v_add3_u32 v40, v40, v56, s73
	v_add3_u32 v41, v41, v55, s73
	v_perm_b32 v91, v17, v42, s72
	v_and_b32_e32 v43, 0xffff0000, v37
	v_lshlrev_b32_e32 v42, 16, v37
	v_perm_b32 v89, v41, v40, s72
	v_perm_b32 v88, v45, v44, s72
	v_and_b32_e32 v41, 0xffff0000, v36
	v_lshlrev_b32_e32 v40, 16, v36
	v_pk_mul_f32 v[36:37], v[16:17], v[42:43] op_sel_hi:[0,1]
	v_and_b32_e32 v43, 0xffff0000, v38
	v_lshlrev_b32_e32 v42, 16, v38
	v_and_b32_e32 v45, 0xffff0000, v39
	v_lshlrev_b32_e32 v44, 16, v39
	v_bfe_u32 v53, v47, 16, 1
	v_bfe_u32 v54, v46, 16, 1
	v_pk_mul_f32 v[40:41], v[16:17], v[40:41] op_sel_hi:[0,1]
	v_pk_mul_f32 v[42:43], v[16:17], v[42:43] op_sel_hi:[0,1]
	v_pk_mul_f32 v[16:17], v[16:17], v[44:45] op_sel_hi:[0,1]
	v_add3_u32 v46, v46, v54, s73
	v_add3_u32 v47, v47, v53, s73
	v_bfe_u32 v38, v17, 16, 1
	v_bfe_u32 v39, v16, 16, 1
	v_perm_b32 v90, v47, v46, s72
	v_bfe_u32 v46, v37, 16, 1
	v_bfe_u32 v47, v36, 16, 1
	v_bfe_u32 v52, v41, 16, 1
	v_bfe_u32 v53, v40, 16, 1
	v_add3_u32 v16, v16, v39, s73
	v_add3_u32 v17, v17, v38, s73
	v_bfe_u32 v44, v43, 16, 1
	v_bfe_u32 v45, v42, 16, 1
	v_add3_u32 v40, v40, v53, s73
	v_add3_u32 v41, v41, v52, s73
	v_add3_u32 v36, v36, v47, s73
	v_add3_u32 v37, v37, v46, s73
	v_perm_b32 v95, v17, v16, s72
	v_mul_f32_e32 v16, 0x3d800000, v18
	v_and_b32_e32 v39, 0xffff0000, v33
; __device__ __forceinline__ bf16 f2bf(float f) { unsigned u = __float_as_uint(f); return (bf16)((u + 0x7fffu + ((u >> 16) & 1u)) >> 16); }
; __device__ __forceinline__ bool run_unit2(LAS unsigned char* lds, const bf16* y0, const float* aux, unsigned* maskg, int b, int g, int tid_in, int wave, int lane) {
;     ...
;     for (int hd = 0; hd < 4; ++hd) {
;         const float wsc = w4[hd] * 0.0625f;
;         lo4[hd] = (w4[hd] >= 0.f) ? 0.f : -INFINITY; hi4[hd] = (w4[hd] >= 0.f) ? INFINITY : 0.f;
; #pragma unroll
;         for (int s = 0; s < 4; ++s) {
;             bf16x8 a = qf[hd][s];
; #pragma unroll
;             for (int j = 0; j < 8; ++j) a[j] = (short)f2bf(__uint_as_float(((unsigned)(unsigned short)a[j]) << 16) * wsc);
;             qf[hd][s] = a;
;         }
	v_lshlrev_b32_e32 v38, 16, v33
	v_add3_u32 v42, v42, v45, s73
	v_add3_u32 v43, v43, v44, s73
	v_perm_b32 v93, v37, v36, s72
	v_perm_b32 v92, v41, v40, s72
	v_and_b32_e32 v37, 0xffff0000, v32
	v_lshlrev_b32_e32 v36, 16, v32
	v_pk_mul_f32 v[32:33], v[16:17], v[38:39] op_sel_hi:[0,1]
	v_and_b32_e32 v41, 0xffff0000, v35
	v_lshlrev_b32_e32 v40, 16, v35
	v_perm_b32 v94, v43, v42, s72
	v_pk_mul_f32 v[36:37], v[16:17], v[36:37] op_sel_hi:[0,1]
	v_and_b32_e32 v39, 0xffff0000, v34
	v_lshlrev_b32_e32 v38, 16, v34
	v_pk_mul_f32 v[34:35], v[16:17], v[40:41] op_sel_hi:[0,1]
	v_bfe_u32 v42, v33, 16, 1
	v_bfe_u32 v43, v32, 16, 1
	v_cndmask_b32_e64 v209, v188, 0, vcc
	v_cndmask_b32_e32 v210, 0, v189, vcc
	v_cmp_le_f32_e32 vcc, 0, v18
	v_pk_mul_f32 v[38:39], v[16:17], v[38:39] op_sel_hi:[0,1]
	v_bfe_u32 v17, v35, 16, 1
	v_bfe_u32 v18, v34, 16, 1
	v_bfe_u32 v44, v37, 16, 1
	v_bfe_u32 v45, v36, 16, 1
	v_add3_u32 v32, v32, v43, s73
	v_add3_u32 v33, v33, v42, s73
	v_bfe_u32 v40, v39, 16, 1
	v_bfe_u32 v41, v38, 16, 1
	v_add3_u32 v36, v36, v45, s73
	v_add3_u32 v37, v37, v44, s73
	v_add3_u32 v18, v34, v18, s73
	v_add3_u32 v17, v35, v17, s73
	v_perm_b32 v97, v33, v32, s72
	v_and_b32_e32 v33, 0xffff0000, v28
	v_lshlrev_b32_e32 v32, 16, v28
	v_and_b32_e32 v35, 0xffff0000, v29
	v_lshlrev_b32_e32 v34, 16, v29
	v_add3_u32 v38, v38, v41, s73
	v_add3_u32 v39, v39, v40, s73
	v_perm_b32 v96, v37, v36, s72
	v_pk_mul_f32 v[32:33], v[16:17], v[32:33] op_sel_hi:[0,1]
	v_pk_mul_f32 v[28:29], v[16:17], v[34:35] op_sel_hi:[0,1]
	v_and_b32_e32 v37, 0xffff0000, v31
	v_lshlrev_b32_e32 v36, 16, v31
	v_perm_b32 v98, v39, v38, s72
	v_and_b32_e32 v35, 0xffff0000, v30
	v_lshlrev_b32_e32 v34, 16, v30
	v_pk_mul_f32 v[30:31], v[16:17], v[36:37] op_sel_hi:[0,1]
	v_bfe_u32 v38, v29, 16, 1
	v_bfe_u32 v39, v28, 16, 1
	v_bfe_u32 v40, v33, 16, 1
	v_bfe_u32 v41, v32, 16, 1
	v_perm_b32 v99, v17, v18, s72
	v_pk_mul_f32 v[34:35], v[16:17], v[34:35] op_sel_hi:[0,1]
	v_bfe_u32 v17, v31, 16, 1
	v_bfe_u32 v18, v30, 16, 1
	v_add3_u32 v32, v32, v41, s73
	v_add3_u32 v33, v33, v40, s73
	v_add3_u32 v28, v28, v39, s73
	v_add3_u32 v29, v29, v38, s73
	v_bfe_u32 v36, v35, 16, 1
	v_bfe_u32 v37, v34, 16, 1
	v_add3_u32 v18, v30, v18, s73
	v_add3_u32 v17, v31, v17, s73
	v_perm_b32 v101, v29, v28, s72
	v_perm_b32 v100, v33, v32, s72
	v_and_b32_e32 v29, 0xffff0000, v24
	v_lshlrev_b32_e32 v28, 16, v24
	v_and_b32_e32 v31, 0xffff0000, v25
	v_lshlrev_b32_e32 v30, 16, v25
	v_and_b32_e32 v33, 0xffff0000, v27
	v_lshlrev_b32_e32 v32, 16, v27
	v_add3_u32 v34, v34, v37, s73
	v_add3_u32 v35, v35, v36, s73
	v_pk_mul_f32 v[28:29], v[16:17], v[28:29] op_sel_hi:[0,1]
	v_pk_mul_f32 v[24:25], v[16:17], v[30:31] op_sel_hi:[0,1]
	v_and_b32_e32 v31, 0xffff0000, v26
	v_lshlrev_b32_e32 v30, 16, v26
	v_pk_mul_f32 v[26:27], v[16:17], v[32:33] op_sel_hi:[0,1]
	v_perm_b32 v103, v17, v18, s72
	v_perm_b32 v102, v35, v34, s72
	v_pk_mul_f32 v[30:31], v[16:17], v[30:31] op_sel_hi:[0,1]
	v_bfe_u32 v17, v27, 16, 1
	v_bfe_u32 v18, v26, 16, 1
	v_bfe_u32 v34, v25, 16, 1
	v_bfe_u32 v35, v24, 16, 1
	v_bfe_u32 v36, v29, 16, 1
	v_bfe_u32 v37, v28, 16, 1
	v_add3_u32 v28, v28, v37, s73
	v_add3_u32 v29, v29, v36, s73
	v_add3_u32 v24, v24, v35, s73
	v_add3_u32 v25, v25, v34, s73
	v_add3_u32 v18, v26, v18, s73
	v_add3_u32 v17, v27, v17, s73
	v_and_b32_e32 v27, 0xffff0000, v21
	v_lshlrev_b32_e32 v26, 16, v21
	v_bfe_u32 v32, v31, 16, 1
	v_bfe_u32 v33, v30, 16, 1
	v_perm_b32 v105, v25, v24, s72
	v_perm_b32 v104, v29, v28, s72
	v_and_b32_e32 v25, 0xffff0000, v20
	v_lshlrev_b32_e32 v24, 16, v20
	v_pk_mul_f32 v[20:21], v[16:17], v[26:27] op_sel_hi:[0,1]
	v_and_b32_e32 v27, 0xffff0000, v22
	v_lshlrev_b32_e32 v26, 16, v22
	v_and_b32_e32 v29, 0xffff0000, v23
	v_lshlrev_b32_e32 v28, 16, v23
	v_add3_u32 v30, v30, v33, s73
	v_add3_u32 v31, v31, v32, s73
	v_perm_b32 v107, v17, v18, s72
	v_pk_mul_f32 v[24:25], v[16:17], v[24:25] op_sel_hi:[0,1]
	v_pk_mul_f32 v[26:27], v[16:17], v[26:27] op_sel_hi:[0,1]
	v_pk_mul_f32 v[16:17], v[16:17], v[28:29] op_sel_hi:[0,1]
	v_perm_b32 v106, v31, v30, s72
	v_bfe_u32 v18, v17, 16, 1
	v_bfe_u32 v22, v16, 16, 1
	v_bfe_u32 v23, v27, 16, 1
	v_bfe_u32 v28, v26, 16, 1
	v_bfe_u32 v29, v21, 16, 1
	v_bfe_u32 v30, v20, 16, 1
	v_add3_u32 v20, v20, v30, s73
	v_add3_u32 v21, v21, v29, s73
	v_add3_u32 v26, v26, v28, s73
	v_add3_u32 v23, v27, v23, s73
	v_add3_u32 v16, v16, v22, s73
	v_add3_u32 v17, v17, v18, s73
	v_cndmask_b32_e64 v212, v188, 0, vcc
	v_cndmask_b32_e32 v213, 0, v189, vcc
	v_bfe_u32 v31, v25, 16, 1
	v_bfe_u32 v32, v24, 16, 1
	v_perm_b32 v111, v17, v16, s72
	v_perm_b32 v110, v23, v26, s72
	v_perm_b32 v109, v21, v20, s72
	v_mul_f32_e32 v16, 0x3d800000, v19
	v_cmp_le_f32_e32 vcc, 0, v19
	v_and_b32_e32 v19, 0xffff0000, v12
	v_lshlrev_b32_e32 v18, 16, v12
	v_and_b32_e32 v21, 0xffff0000, v13
	v_lshlrev_b32_e32 v20, 16, v13
	v_and_b32_e32 v23, 0xffff0000, v15
	v_lshlrev_b32_e32 v22, 16, v15
	v_add3_u32 v24, v24, v32, s73
	v_add3_u32 v25, v25, v31, s73
	v_pk_mul_f32 v[18:19], v[16:17], v[18:19] op_sel_hi:[0,1]
	v_pk_mul_f32 v[12:13], v[16:17], v[20:21] op_sel_hi:[0,1]
	v_and_b32_e32 v21, 0xffff0000, v14
	v_lshlrev_b32_e32 v20, 16, v14
; __device__ __forceinline__ bf16 f2bf(float f) { unsigned u = __float_as_uint(f); return (bf16)((u + 0x7fffu + ((u >> 16) & 1u)) >> 16); }
; #define DSA2_LOADK(dst, kt_) do { _Pragma("unroll") for (int s = 0; s < 4; ++s) dst[s] = *(const bf16x8*)(kp + (size_t)(32 * (kt_)) * Y0P + 16 * s); } while (0)
; template <int STAGE>
; __device__ __forceinline__ void pass2(LAS unsigned char* lds, const bf16* kbase, int g, int t0, const bf16x8 (&qf)[4][4], const f32x4 lo4, const f32x4 hi4, int wave, int r, int h2) {
;     ...
;     int kt = wave;
;     if (kt <= g) DSA2_LOADK(kf, kt);
;     for (;;) {
;         if (kt > g) break;
;         if (kt + 8 <= g) DSA2_LOADK(kn, kt + 8);
; __device__ __forceinline__ bool run_unit2(LAS unsigned char* lds, const bf16* y0, const float* aux, unsigned* maskg, int b, int g, int tid_in, int wave, int lane) {
;     ...
;     for (int hd = 0; hd < 4; ++hd) {
;         const float wsc = w4[hd] * 0.0625f;
;         lo4[hd] = (w4[hd] >= 0.f) ? 0.f : -INFINITY; hi4[hd] = (w4[hd] >= 0.f) ? INFINITY : 0.f;
; #pragma unroll
;         for (int s = 0; s < 4; ++s) {
;             bf16x8 a = qf[hd][s];
; #pragma unroll
;             for (int j = 0; j < 8; ++j) a[j] = (short)f2bf(__uint_as_float(((unsigned)(unsigned short)a[j]) << 16) * wsc);
;             qf[hd][s] = a;
;         }
;     }
;     const bf16* kbase = y0 + rowbase * (size_t)Y0P + Y0_IK;
	v_pk_mul_f32 v[14:15], v[16:17], v[22:23] op_sel_hi:[0,1]
	v_perm_b32 v108, v25, v24, s72
	v_pk_mul_f32 v[20:21], v[16:17], v[20:21] op_sel_hi:[0,1]
	v_bfe_u32 v17, v15, 16, 1
	v_bfe_u32 v22, v14, 16, 1
	v_bfe_u32 v25, v13, 16, 1
	v_bfe_u32 v26, v12, 16, 1
	v_bfe_u32 v27, v19, 16, 1
	v_bfe_u32 v28, v18, 16, 1
	v_add3_u32 v18, v18, v28, s73
	v_add3_u32 v19, v19, v27, s73
	v_add3_u32 v12, v12, v26, s73
	v_add3_u32 v13, v13, v25, s73
	v_add3_u32 v14, v14, v22, s73
	v_add3_u32 v15, v15, v17, s73
	v_perm_b32 v115, v15, v14, s72
	v_perm_b32 v113, v13, v12, s72
	v_perm_b32 v112, v19, v18, s72
	v_and_b32_e32 v13, 0xffff0000, v8
	v_lshlrev_b32_e32 v12, 16, v8
	v_and_b32_e32 v15, 0xffff0000, v9
	v_lshlrev_b32_e32 v14, 16, v9
	v_and_b32_e32 v19, 0xffff0000, v11
	v_lshlrev_b32_e32 v18, 16, v11
	v_bfe_u32 v23, v21, 16, 1
	v_bfe_u32 v24, v20, 16, 1
	v_pk_mul_f32 v[12:13], v[16:17], v[12:13] op_sel_hi:[0,1]
	v_pk_mul_f32 v[8:9], v[16:17], v[14:15] op_sel_hi:[0,1]
	v_and_b32_e32 v15, 0xffff0000, v10
	v_lshlrev_b32_e32 v14, 16, v10
	v_pk_mul_f32 v[10:11], v[16:17], v[18:19] op_sel_hi:[0,1]
	v_add3_u32 v20, v20, v24, s73
	v_add3_u32 v21, v21, v23, s73
	v_pk_mul_f32 v[14:15], v[16:17], v[14:15] op_sel_hi:[0,1]
	v_bfe_u32 v17, v11, 16, 1
	v_bfe_u32 v18, v10, 16, 1
	v_bfe_u32 v23, v13, 16, 1
	v_bfe_u32 v24, v12, 16, 1
	v_perm_b32 v114, v21, v20, s72
	v_bfe_u32 v21, v9, 16, 1
	v_bfe_u32 v22, v8, 16, 1
	v_add3_u32 v12, v12, v24, s73
	v_add3_u32 v13, v13, v23, s73
	v_add3_u32 v10, v10, v18, s73
	v_add3_u32 v11, v11, v17, s73
	v_add3_u32 v8, v8, v22, s73
	v_add3_u32 v9, v9, v21, s73
	v_perm_b32 v119, v11, v10, s72
	v_perm_b32 v116, v13, v12, s72
	v_and_b32_e32 v11, 0xffff0000, v5
	v_lshlrev_b32_e32 v10, 16, v5
	v_and_b32_e32 v13, 0xffff0000, v7
	v_lshlrev_b32_e32 v12, 16, v7
	v_perm_b32 v117, v9, v8, s72
	v_and_b32_e32 v9, 0xffff0000, v4
	v_lshlrev_b32_e32 v8, 16, v4
	v_pk_mul_f32 v[4:5], v[16:17], v[10:11] op_sel_hi:[0,1]
	v_and_b32_e32 v11, 0xffff0000, v6
	v_lshlrev_b32_e32 v10, 16, v6
	v_pk_mul_f32 v[6:7], v[16:17], v[12:13] op_sel_hi:[0,1]
	v_bfe_u32 v19, v15, 16, 1
	v_bfe_u32 v20, v14, 16, 1
	v_pk_mul_f32 v[8:9], v[16:17], v[8:9] op_sel_hi:[0,1]
	v_bfe_u32 v12, v7, 16, 1
	v_bfe_u32 v13, v6, 16, 1
	v_add3_u32 v14, v14, v20, s73
	v_add3_u32 v15, v15, v19, s73
	v_pk_mul_f32 v[10:11], v[16:17], v[10:11] op_sel_hi:[0,1]
	v_bfe_u32 v17, v5, 16, 1
	v_bfe_u32 v18, v4, 16, 1
	v_bfe_u32 v19, v9, 16, 1
	v_bfe_u32 v20, v8, 16, 1
	v_add3_u32 v6, v6, v13, s73
	v_add3_u32 v7, v7, v12, s73
	v_add3_u32 v8, v8, v20, s73
	v_add3_u32 v9, v9, v19, s73
	v_add3_u32 v4, v4, v18, s73
	v_add3_u32 v5, v5, v17, s73
	v_perm_b32 v123, v7, v6, s72
	v_and_b32_e32 v7, 0xffff0000, v1
	v_lshlrev_b32_e32 v6, 16, v1
	v_perm_b32 v118, v15, v14, s72
	v_bfe_u32 v14, v11, 16, 1
	v_bfe_u32 v15, v10, 16, 1
	v_perm_b32 v121, v5, v4, s72
	v_perm_b32 v120, v9, v8, s72
	v_and_b32_e32 v5, 0xffff0000, v0
	v_lshlrev_b32_e32 v4, 16, v0
	v_pk_mul_f32 v[0:1], v[16:17], v[6:7] op_sel_hi:[0,1]
	v_and_b32_e32 v7, 0xffff0000, v2
	v_lshlrev_b32_e32 v6, 16, v2
	v_and_b32_e32 v9, 0xffff0000, v3
	v_lshlrev_b32_e32 v8, 16, v3
	v_add3_u32 v10, v10, v15, s73
	v_add3_u32 v11, v11, v14, s73
	v_pk_mul_f32 v[4:5], v[16:17], v[4:5] op_sel_hi:[0,1]
	v_pk_mul_f32 v[6:7], v[16:17], v[6:7] op_sel_hi:[0,1]
	v_pk_mul_f32 v[2:3], v[16:17], v[8:9] op_sel_hi:[0,1]
	v_bfe_u32 v12, v1, 16, 1
	v_bfe_u32 v13, v0, 16, 1
	v_perm_b32 v122, v11, v10, s72
	v_bfe_u32 v8, v3, 16, 1
	v_bfe_u32 v9, v2, 16, 1
	v_bfe_u32 v10, v7, 16, 1
	v_bfe_u32 v11, v6, 16, 1
	v_bfe_u32 v14, v5, 16, 1
	v_bfe_u32 v15, v4, 16, 1
	v_add3_u32 v0, v0, v13, s73
	v_add3_u32 v1, v1, v12, s73
	v_add3_u32 v4, v4, v15, s73
	v_add3_u32 v5, v5, v14, s73
	v_add3_u32 v6, v6, v11, s73
	v_add3_u32 v7, v7, v10, s73
	v_add3_u32 v2, v2, v9, s73
	v_add3_u32 v3, v3, v8, s73
	v_perm_b32 v125, v1, v0, s72
	v_lshl_add_u64 v[0:1], s[80:81], 0, v[176:177]
	v_cndmask_b32_e64 v214, v188, 0, vcc
	v_cndmask_b32_e32 v215, 0, v189, vcc
	v_perm_b32 v127, v3, v2, s72
	v_perm_b32 v126, v7, v6, s72
	v_perm_b32 v124, v5, v4, s72
	v_lshl_add_u64 v[178:179], v[0:1], 0, v[50:51]
	s_cbranch_scc1 .LBB0_804
	v_lshl_add_u64 v[0:1], v[178:179], 0, s[36:37]
	global_load_dwordx4 v[140:143], v[0:1], off
	global_load_dwordx4 v[136:139], v[0:1], off offset:32
	global_load_dwordx4 v[132:135], v[0:1], off offset:64
	global_load_dwordx4 v[128:131], v[0:1], off offset:96
	v_lshl_add_u64 v[0:1], v[48:49], 1, s[78:79]
	v_lshl_add_u64 v[0:1], v[0:1], 0, v[176:177]
	v_mad_u32_u24 v204, v218, s26, 0
	v_lshl_add_u64 v[180:181], s[34:35], 0, v[0:1]
	s_sub_i32 s0, 0, s64
	s_mov_b32 s1, s30
	s_mov_b32 s6, s92
	v_readlane_b32 s98, v254, 24
	s_cmp_lt_u32 s98, 4
	s_cbranch_scc1 .Lp4stag0
	s_sleep 14
.Lp4stag0:
.LBB0_785:
	s_add_i32 s4, s1, -8
	s_cmp_le_u32 s4, s64
	s_cselect_b64 s[2:3], -1, 0
	s_cmp_gt_u32 s4, s64
	s_cbranch_scc1 .LBB0_787
	v_add_co_u32_e32 v0, vcc, 0xffe40000, v180
	s_nop 1
	v_addc_co_u32_e32 v1, vcc, -1, v181, vcc
	global_load_dwordx4 v[156:159], v[0:1], off offset:-96
	global_load_dwordx4 v[152:155], v[0:1], off offset:-64
	global_load_dwordx4 v[148:151], v[0:1], off offset:-32
	global_load_dwordx4 v[144:147], v[0:1], off

; #define LAS __attribute__((address_space(3)))
; #define DSA2_LOADK(dst, kt_) do { _Pragma("unroll") for (int s = 0; s < 4; ++s) dst[s] = *(const bf16x8*)(kp + (size_t)(32 * (kt_)) * Y0P + 16 * s); } while (0)
; template <int STAGE>
; __device__ __forceinline__ void pass2(LAS unsigned char* lds, const bf16* kbase, int g, int t0, const bf16x8 (&qf)[4][4], const f32x4 lo4, const f32x4 hi4, int wave, int r, int h2) {
;     ...
;     const int tq = t0 + r;
;     const int tb = (STAGE == 1) ? ((const LAS int*)(lds + OFF2_TB))[r] : 0;
;     bf16x8 kf[4], kn[4];
;     const bf16* kp = kbase + (size_t)r * Y0P + 8 * h2;
;     ...
;     int kt = wave;
;     if (kt <= g) DSA2_LOADK(kf, kt);
;     for (;;) {
;         if (kt > g) break;
;         if (kt + 8 <= g) DSA2_LOADK(kn, kt + 8);
.LBB0_822:
	s_or_b64 exec, exec, s[4:5]
	s_andn2_b64 vcc, exec, s[82:83]
	s_waitcnt lgkmcnt(0)
	s_barrier
	s_cbranch_vccnz .LBB0_880
	v_lshl_add_u64 v[0:1], v[178:179], 0, s[36:37]
	global_load_dwordx4 v[140:143], v[0:1], off
	global_load_dwordx4 v[136:139], v[0:1], off offset:32
	global_load_dwordx4 v[132:135], v[0:1], off offset:64
	global_load_dwordx4 v[128:131], v[0:1], off offset:96
	v_lshlrev_b32_e32 v0, 2, v218
	v_add_u32_e32 v1, 0, v0
	v_add_u32_e32 v1, 0x18100, v1
	ds_read_b32 v222, v1
	s_add_i32 s0, 0, 0x18200
	v_lshlrev_b32_e32 v1, 9, v219
	v_lshlrev_b32_e32 v2, 4, v218
	v_add_u32_e32 v224, s0, v0
	v_mov_b32_e32 v0, s27
	v_add3_u32 v223, s65, v1, v2
	v_lshlrev_b32_e32 v219, 2, v219
	v_lshl_add_u32 v225, v218, 11, 0
	v_cmp_gt_u32_e64 s[84:85], 32, v217
	v_mad_u32_u24 v217, v218, s24, v0
	v_readlane_b32 s0, v254, 24
	s_waitcnt lgkmcnt(0)
	v_sub_u32_e32 v0, 0xcf, v222
	v_add_u32_e32 v0, 0x340, v0
	v_lshlrev_b32_e32 v0, 20, v0
	v_add_u32_e32 v0, 0x7fffffff, v0
	v_add_u32_e32 v1, 0x100000, v0
	v_add_u32_e32 v2, 0x230, v222
	v_lshlrev_b32_e32 v2, 20, v2
	v_add_u32_e32 v3, 0x100000, v2
	v_mov_b32_e32 v4, 0xff800000
	v_bfrev_b32_e32 v5, 1
	v_mov_b32_e32 v6, 1
	v_mov_b32_e32 v7, 0x7fc00000
	v_mov_b32_e32 v8, 0x7fffffff
	v_cmp_gt_i32_e32 vcc, 0, v222
	s_nop 1
	v_cndmask_b32_e32 v252, v0, v4, vcc
	v_cmp_eq_u32_e32 vcc, 0xcf, v222
	s_nop 1
	v_cndmask_b32_e32 v252, v252, v5, vcc
	v_cmp_lt_i32_e32 vcc, 0xcf, v222
	s_nop 1
	v_cndmask_b32_e32 v252, v252, v6, vcc
	v_cmp_lt_i32_e32 vcc, 0x10f, v222
	s_nop 1
	v_cndmask_b32_e32 v252, v252, v3, vcc
	v_cmp_eq_u32_e32 vcc, 0x1df, v222
	s_nop 1
	v_cndmask_b32_e32 v252, v252, v7, vcc
	v_cmp_gt_i32_e32 vcc, 1, v222
	s_nop 1
	v_cndmask_b32_e32 v253, v1, v4, vcc
	v_cmp_lt_i32_e32 vcc, 0xcf, v222
	s_nop 1
	v_cndmask_b32_e32 v253, v253, v6, vcc
	v_cmp_lt_i32_e32 vcc, 0x110, v222
	s_nop 1
	v_cndmask_b32_e32 v253, v253, v2, vcc
	v_cmp_lt_i32_e32 vcc, 0xcf, v222
	s_nop 1
	v_cndmask_b32_e32 v232, v8, v222, vcc
	v_cmp_lt_i32_e32 vcc, 0x10f, v222
	s_nop 1
	v_cndmask_b32_e32 v232, v232, v8, vcc
	s_cmp_lt_u32 s0, 4
	s_cbranch_scc1 .Lp4stag1
	s_sleep 14
.Lp4stag1:
.LBB0_824:
	s_add_i32 s1, s0, 8
	s_cmp_le_u32 s1, s64
	s_cselect_b64 s[4:5], -1, 0
	s_cmp_gt_u32 s1, s64
	s_cbranch_scc1 .LBB0_826
	s_lshl_b32 s6, s1, 5
	v_mad_u64_u32 v[0:1], s[6:7], s6, v187, v[178:179]
	global_load_dwordx4 v[156:159], v[0:1], off
	global_load_dwordx4 v[152:155], v[0:1], off offset:32
	global_load_dwordx4 v[148:151], v[0:1], off offset:64
	global_load_dwordx4 v[144:147], v[0:1], off offset:96
